# removed never-taken branch tests in the max-phase chain (one live test per tile instead of two)
# speedup vs baseline: 1.0100x; 1.0100x over previous
.Ltri1_done:
	s_cmp_lg_u32 s36, 0x60000
	s_cselect_b64 s[52:53], -1, 0
	s_cmp_eq_u32 s36, 0x60000
	s_cselect_b32 s23, s27, s55
	s_cselect_b32 s22, s26, s54
	s_setprio 0
	v_readfirstlane_b32 s24, v224
	s_mov_b32 m0, s24
	v_readfirstlane_b32 s24, v225
	global_load_lds_dwordx4 v223, s[22:23]
	s_mov_b32 m0, s24
	v_readfirstlane_b32 s24, v213
	global_load_lds_dwordx4 v210, s[22:23]
	s_mov_b32 m0, s24
	v_readfirstlane_b32 s24, v215
	global_load_lds_dwordx4 v212, s[22:23]
	s_mov_b32 m0, s24
	s_nop 0
	global_load_lds_dwordx4 v214, s[22:23]
	v_mov_b32_e32 v243, 0xff800000
	s_not_b64 s[22:23], s[2:3]
	s_andn2_b64 vcc, exec, s[2:3]
	v_mov_b32_e32 v1, 0xff800000
	s_cbranch_vccz .LBB1_64
.LBB1_13:
	v_mov_b32_e32 v241, 0xff800000
	s_and_b64 vcc, exec, s[16:17]
	v_mov_b32_e32 v242, 0xff800000
	s_cbranch_vccz .LBB1_66
.LBB1_14:
.LBB1_15:
	v_mov_b32_e32 v239, 0xff800000
	s_and_b64 vcc, exec, s[18:19]
	v_mov_b32_e32 v240, 0xff800000
	s_cbranch_vccz .LBB1_68
.LBB1_16:
.LBB1_17:
	v_mov_b32_e32 v237, 0xff800000
	s_and_b64 vcc, exec, s[20:21]
	v_mov_b32_e32 v238, 0xff800000
	s_cbranch_vccz .LBB1_70
.LBB1_18:
	s_branch .LBB1_20

.LBB1_38:
	s_setprio 0
	v_mov_b32_e32 v16, 0xff800000
	s_and_b64 vcc, exec, s[18:19]
	v_mov_b32_e32 v1, 0xff800000
	s_cbranch_vccz .LBB1_75
.LBB1_40:
	v_mov_b32_e32 v14, 0xff800000
	s_and_b64 vcc, exec, s[20:21]
	v_mov_b32_e32 v15, 0xff800000
	s_cbranch_vccz .LBB1_77
.LBB1_41:
.LBB1_42:
	v_mov_b32_e32 v12, 0xff800000
	s_and_b64 vcc, exec, s[22:23]
	v_mov_b32_e32 v13, 0xff800000
	s_cbranch_vccz .LBB1_79
.LBB1_43:
.LBB1_44:
	v_mov_b32_e32 v9, 0xff800000
	s_and_b64 vcc, exec, s[24:25]
	v_mov_b32_e32 v11, 0xff800000
	s_cbranch_vccz .LBB1_81

.LBB1_64:
	v_max3_f32 v1, v66, v67, v68
	v_max3_f32 v1, v1, v69, v70
	v_max3_f32 v1, v1, v71, v72
	v_max_f32_e32 v1, v1, v73
.LBB1_65:
	v_max3_f32 v3, v74, v75, v76
	v_max3_f32 v3, v3, v77, v78
	v_max3_f32 v3, v3, v79, v80
	v_max_f32_e32 v243, v3, v81
	v_mov_b32_e32 v241, 0xff800000
	s_and_b64 vcc, exec, s[16:17]
	v_mov_b32_e32 v242, 0xff800000
	s_cbranch_vccnz .LBB1_14
.LBB1_66:
	v_max3_f32 v3, v50, v51, v52
	v_max3_f32 v3, v3, v53, v54
	v_max3_f32 v3, v3, v55, v56
	v_max_f32_e32 v242, v3, v57
.LBB1_67:
	v_max3_f32 v3, v58, v59, v60
	v_max3_f32 v3, v3, v61, v62
	v_max3_f32 v3, v3, v63, v64
	v_max_f32_e32 v241, v3, v65
	v_mov_b32_e32 v239, 0xff800000
	s_and_b64 vcc, exec, s[18:19]
	v_mov_b32_e32 v240, 0xff800000
	s_cbranch_vccnz .LBB1_16
.LBB1_68:
	v_max3_f32 v3, v34, v35, v36
	v_max3_f32 v3, v3, v37, v38
	v_max3_f32 v3, v3, v39, v40
	v_max_f32_e32 v240, v3, v41
.LBB1_69:
	v_max3_f32 v3, v42, v43, v44
	v_max3_f32 v3, v3, v45, v46
	v_max3_f32 v3, v3, v47, v48
	v_max_f32_e32 v239, v3, v49
	v_mov_b32_e32 v237, 0xff800000
	s_and_b64 vcc, exec, s[20:21]
	v_mov_b32_e32 v238, 0xff800000
	s_cbranch_vccnz .LBB1_18
.LBB1_70:
	v_max3_f32 v3, v18, v19, v20
	v_max3_f32 v3, v3, v21, v22
	v_max3_f32 v3, v3, v23, v24
	v_max_f32_e32 v238, v3, v25
	s_branch .LBB1_19

.LBB1_75:
	v_max3_f32 v1, v66, v67, v68
	v_max3_f32 v1, v1, v69, v70
	v_max3_f32 v1, v1, v71, v72
	v_max_f32_e32 v1, v1, v73
.LBB1_76:
	v_max3_f32 v3, v74, v75, v76
	v_max3_f32 v3, v3, v77, v78
	v_max3_f32 v3, v3, v79, v80
	v_max_f32_e32 v16, v3, v81
	v_mov_b32_e32 v14, 0xff800000
	s_and_b64 vcc, exec, s[20:21]
	v_mov_b32_e32 v15, 0xff800000
	s_cbranch_vccnz .LBB1_41
.LBB1_77:
	v_max3_f32 v3, v50, v51, v52
	v_max3_f32 v3, v3, v53, v54
	v_max3_f32 v3, v3, v55, v56
	v_max_f32_e32 v15, v3, v57
.LBB1_78:
	v_max3_f32 v3, v58, v59, v60
	v_max3_f32 v3, v3, v61, v62
	v_max3_f32 v3, v3, v63, v64
	v_max_f32_e32 v14, v3, v65
	v_mov_b32_e32 v12, 0xff800000
	s_and_b64 vcc, exec, s[22:23]
	v_mov_b32_e32 v13, 0xff800000
	s_cbranch_vccnz .LBB1_43
.LBB1_79:
	v_max3_f32 v3, v34, v35, v36
	v_max3_f32 v3, v3, v37, v38
	v_max3_f32 v3, v3, v39, v40
	v_max_f32_e32 v13, v3, v41
.LBB1_80:
	v_max3_f32 v3, v42, v43, v44
	v_max3_f32 v3, v3, v45, v46
	v_max3_f32 v3, v3, v47, v48
	v_max_f32_e32 v12, v3, v49
	v_mov_b32_e32 v9, 0xff800000
	s_and_b64 vcc, exec, s[24:25]
	v_mov_b32_e32 v11, 0xff800000
	s_cbranch_vccnz .LBB1_45
.LBB1_81:
	v_max3_f32 v3, v18, v19, v20
	v_max3_f32 v3, v3, v21, v22
	v_max3_f32 v3, v3, v23, v24
	v_max_f32_e32 v11, v3, v25
	s_branch .LBB1_46
